# H3 epilogue: eight per-unit output-norm gain loads hoisted ~280 instructions ahead into v[152:183] (were eight load->vmcnt(0)->use round trips per unit); one wait at first use
# baseline (speedup 1.0000x reference)
.LBB0_763:
	s_and_b32 s3, s9, 0xf0
	s_and_b32 s9, s10, 0x7fffff00
	s_bfe_u32 s2, s10, 0x40004
	s_or_b32 s3, s9, s3
	s_or_b32 s2, s3, s2
	s_lshl_b32 s2, s2, 1
	s_add_i32 s9, s2, s6
	s_ashr_i32 s2, s9, 9
	s_ashr_i32 s3, s2, 31
	s_lshl_b32 s10, s9, 6
	s_lshl_b64 s[2:3], s[2:3], 11
	s_and_b32 s10, s10, 0x7c0
	s_or_b32 s2, s2, s10
	v_mov_b32_e32 v37, s3
	v_or_b32_e32 v36, s2, v52
	s_lshl_b32 s2, s9, 2
	s_and_b32 s9, s2, 0x780
	v_lshlrev_b64 v[80:81], 12, v[36:37]
	v_lshl_or_b32 v80, s9, 1, v80
	v_lshl_add_u64 v[36:37], v[56:57], 0, v[80:81]
	global_load_dwordx4 v[48:51], v[36:37], off
	global_load_dwordx4 v[44:47], v[36:37], off offset:64
	global_load_dwordx4 v[40:43], v[36:37], off offset:128
	s_nop 0
	global_load_dwordx4 v[36:39], v[36:37], off offset:192
	v_lshl_add_u64 v[66:67], v[58:59], 0, v[80:81]
	v_lshl_add_u64 v[88:89], v[60:61], 0, v[80:81]
	global_load_dwordx2 v[100:101], v[66:67], off
	global_load_dwordx2 v[82:83], v[88:89], off
	global_load_dwordx2 v[106:107], v[66:67], off offset:32
	global_load_dwordx2 v[78:79], v[88:89], off offset:32
	global_load_dwordx2 v[98:99], v[66:67], off offset:64
	global_load_dwordx2 v[76:77], v[88:89], off offset:64
	global_load_dwordx2 v[96:97], v[66:67], off offset:96
	global_load_dwordx2 v[74:75], v[88:89], off offset:96
	global_load_dwordx2 v[104:105], v[66:67], off offset:128
	global_load_dwordx2 v[72:73], v[88:89], off offset:128
	global_load_dwordx2 v[108:109], v[66:67], off offset:160
	global_load_dwordx2 v[70:71], v[88:89], off offset:160
	global_load_dwordx2 v[112:113], v[66:67], off offset:192
	global_load_dwordx2 v[68:69], v[88:89], off offset:192
	global_load_dwordx2 v[116:117], v[66:67], off offset:224
	s_nop 0
	global_load_dwordx2 v[66:67], v[88:89], off offset:224
	ds_read_b128 v[88:91], v53
	ds_read_b128 v[92:95], v53 offset:64
	s_mov_b32 s2, 0xf800000
	s_lshl_b32 s34, s9, 2
	s_mov_b32 s9, s8
	s_mov_b32 s10, s7
	s_waitcnt vmcnt(0) lgkmcnt(0)
	v_lshl_add_u64 v[184:185], v[62:63], 0, s[34:35]
	global_load_dwordx4 v[152:155], v[184:185], off
	global_load_dwordx4 v[156:159], v[184:185], off offset:64
	global_load_dwordx4 v[160:163], v[184:185], off offset:128
	global_load_dwordx4 v[164:167], v[184:185], off offset:192
	global_load_dwordx4 v[168:171], v[184:185], off offset:256
	global_load_dwordx4 v[172:175], v[184:185], off offset:320
	global_load_dwordx4 v[176:179], v[184:185], off offset:384
	global_load_dwordx4 v[180:183], v[184:185], off offset:448
	v_mfma_f32_16x16x32_bf16 v[88:91], v[88:91], v[48:51], 0
	ds_read_b128 v[118:121], v53 offset:8768
	ds_read_b128 v[122:125], v53 offset:13120
	v_mfma_f32_16x16x32_bf16 v[88:91], v[92:95], v[44:47], v[88:91]
	ds_read_b128 v[92:95], v53 offset:128
	s_waitcnt lgkmcnt(0)
	v_mfma_f32_16x16x32_bf16 v[88:91], v[92:95], v[40:43], v[88:91]
	ds_read_b128 v[92:95], v53 offset:192
	s_waitcnt lgkmcnt(0)
	v_mfma_f32_16x16x32_bf16 v[88:91], v[92:95], v[36:39], v[88:91]
	v_lshlrev_b32_e32 v94, 16, v100
	v_and_b32_e32 v95, 0xffff0000, v100
	v_lshlrev_b32_e32 v92, 16, v101
	v_and_b32_e32 v93, 0xffff0000, v101
	s_nop 3
	v_pk_add_f32 v[92:93], v[90:91], v[92:93]
	v_pk_add_f32 v[94:95], v[88:89], v[94:95]
	ds_read_b128 v[88:91], v53 offset:4352
	ds_read_b128 v[100:103], v53 offset:4416
	s_waitcnt lgkmcnt(1)
	v_mfma_f32_16x16x32_bf16 v[88:91], v[88:91], v[48:51], 0
	s_waitcnt lgkmcnt(0)
	v_mfma_f32_16x16x32_bf16 v[88:91], v[100:103], v[44:47], v[88:91]
	ds_read_b128 v[100:103], v53 offset:4480
	s_waitcnt lgkmcnt(0)
	v_mfma_f32_16x16x32_bf16 v[88:91], v[100:103], v[40:43], v[88:91]
	ds_read_b128 v[100:103], v53 offset:4544
	s_waitcnt lgkmcnt(0)
	v_mfma_f32_16x16x32_bf16 v[100:103], v[100:103], v[36:39], v[88:91]
	s_nop 4
	v_lshlrev_b32_e32 v90, 16, v106
	v_and_b32_e32 v91, 0xffff0000, v106
	v_lshlrev_b32_e32 v88, 16, v107
	v_and_b32_e32 v89, 0xffff0000, v107
	v_pk_add_f32 v[90:91], v[100:101], v[90:91]
	v_pk_add_f32 v[88:89], v[102:103], v[88:89]
	v_mov_b32_e32 v102, v95
	v_mov_b32_e32 v103, v91
	v_mov_b32_e32 v100, v94
	v_mov_b32_e32 v101, v90
	v_pk_mul_f32 v[102:103], v[102:103], v[102:103]
	v_mov_b32_e32 v106, v93
	v_mov_b32_e32 v107, v89
	v_pk_fma_f32 v[100:101], v[100:101], v[100:101], v[102:103]
	v_mov_b32_e32 v102, v92
	v_mov_b32_e32 v103, v88
	v_pk_mul_f32 v[106:107], v[106:107], v[106:107]
	s_nop 0
	v_pk_fma_f32 v[102:103], v[102:103], v[102:103], v[106:107]
	s_nop 0
	v_pk_add_f32 v[110:111], v[100:101], v[102:103]
	ds_read_b128 v[100:103], v53 offset:8704
	s_waitcnt lgkmcnt(0)
	v_mfma_f32_16x16x32_bf16 v[100:103], v[100:103], v[48:51], 0
	v_pk_add_f32 v[110:111], v[110:111], v[110:111] op_sel:[0,1] op_sel_hi:[1,0]
	v_mfma_f32_16x16x32_bf16 v[100:103], v[118:121], v[44:47], v[100:103]
	ds_read_b128 v[118:121], v53 offset:8832
	s_waitcnt lgkmcnt(0)
	v_mfma_f32_16x16x32_bf16 v[100:103], v[118:121], v[40:43], v[100:103]
	ds_read_b128 v[118:121], v53 offset:8896
	s_waitcnt lgkmcnt(0)
	v_mfma_f32_16x16x32_bf16 v[118:121], v[118:121], v[36:39], v[100:103]
	s_nop 4
	v_lshlrev_b32_e32 v102, 16, v98
	v_and_b32_e32 v103, 0xffff0000, v98
	v_lshlrev_b32_e32 v98, 16, v99
	v_and_b32_e32 v99, 0xffff0000, v99
	v_pk_add_f32 v[100:101], v[120:121], v[98:99]
	v_pk_add_f32 v[102:103], v[118:119], v[102:103]
	ds_read_b128 v[118:121], v53 offset:13056
	s_waitcnt lgkmcnt(0)
	v_mfma_f32_16x16x32_bf16 v[118:121], v[118:121], v[48:51], 0
	v_mul_f32_e64 v98, v102, v102
	v_mul_f32_e64 v99, v103, v103
	v_pk_mul_f32 v[106:107], v[100:101], v[100:101]
	v_mfma_f32_16x16x32_bf16 v[118:121], v[122:125], v[44:47], v[118:121]
	ds_read_b128 v[122:125], v53 offset:13184
	v_pk_mov_b32 v[114:115], v[98:99], v[106:107] op_sel:[1,0]
	v_mov_b32_e32 v99, v107
	s_waitcnt lgkmcnt(0)
	v_mfma_f32_16x16x32_bf16 v[118:121], v[122:125], v[40:43], v[118:121]
	ds_read_b128 v[122:125], v53 offset:13248
	v_pk_add_f32 v[114:115], v[114:115], v[98:99]
	v_lshlrev_b32_e32 v98, 16, v96
	s_waitcnt lgkmcnt(0)
	v_mfma_f32_16x16x32_bf16 v[118:121], v[122:125], v[36:39], v[118:121]
	v_and_b32_e32 v99, 0xffff0000, v96
	v_lshlrev_b32_e32 v96, 16, v97
	v_and_b32_e32 v97, 0xffff0000, v97
	s_nop 4
	v_pk_add_f32 v[96:97], v[120:121], v[96:97]
	v_pk_add_f32 v[98:99], v[118:119], v[98:99]
	ds_read_b128 v[118:121], v53 offset:17408
	ds_read_b128 v[122:125], v53 offset:17472
	s_waitcnt lgkmcnt(1)
	v_mfma_f32_16x16x32_bf16 v[118:121], v[118:121], v[48:51], 0
	v_lshlrev_b32_e32 v106, 16, v104
	v_and_b32_e32 v107, 0xffff0000, v104
	v_lshlrev_b32_e32 v104, 16, v105
	s_waitcnt lgkmcnt(0)
	v_mfma_f32_16x16x32_bf16 v[118:121], v[122:125], v[44:47], v[118:121]
	ds_read_b128 v[122:125], v53 offset:17536
	v_and_b32_e32 v105, 0xffff0000, v105
	v_pk_add_f32 v[114:115], v[114:115], v[114:115] op_sel:[0,1] op_sel_hi:[1,0]
	s_waitcnt lgkmcnt(0)
	v_mfma_f32_16x16x32_bf16 v[118:121], v[122:125], v[40:43], v[118:121]
	ds_read_b128 v[122:125], v53 offset:17600
	s_waitcnt lgkmcnt(0)
	v_mfma_f32_16x16x32_bf16 v[118:121], v[122:125], v[36:39], v[118:121]
	ds_read_b128 v[124:127], v53 offset:21824
	s_nop 6
	v_pk_add_f32 v[106:107], v[118:119], v[106:107]
	s_nop 0
	v_mul_f32_e32 v2, v106, v106
	v_mul_f32_e32 v118, v107, v107
	v_pk_add_f32 v[104:105], v[120:121], v[104:105]
	v_mov_b32_e32 v111, v2
	v_mov_b32_e32 v115, v118
	v_mul_f32_e32 v2, v99, v99
	v_mul_f32_e32 v119, v104, v104
	v_pk_add_f32 v[110:111], v[110:111], v[114:115]
	v_pk_fma_f32 v[114:115], v[98:99], v[98:99], v[2:3] op_sel_hi:[1,1,0]
	v_mul_f32_e32 v2, v97, v97
	v_mul_f32_e32 v120, v105, v105
	v_mov_b32_e32 v115, v119
	v_pk_fma_f32 v[118:119], v[96:97], v[96:97], v[2:3] op_sel_hi:[1,1,0]
	s_nop 0
	v_mov_b32_e32 v119, v120
	ds_read_b128 v[120:123], v53 offset:21760
	s_waitcnt lgkmcnt(0)
	v_mfma_f32_16x16x32_bf16 v[120:123], v[120:123], v[48:51], 0
	v_add_f32_e64 v114, v114, v118
	v_add_f32_e64 v115, v115, v119
	v_pk_add_f32 v[118:119], v[110:111], v[114:115]
	v_mfma_f32_16x16x32_bf16 v[120:123], v[124:127], v[44:47], v[120:123]
	ds_read_b128 v[124:127], v53 offset:21888
	v_lshlrev_b32_e32 v110, 16, v108
	v_and_b32_e32 v111, 0xffff0000, v108
	s_waitcnt lgkmcnt(0)
	v_mfma_f32_16x16x32_bf16 v[120:123], v[124:127], v[40:43], v[120:123]
	ds_read_b128 v[124:127], v53 offset:21952
	v_lshlrev_b32_e32 v108, 16, v109
	v_and_b32_e32 v109, 0xffff0000, v109
	s_waitcnt lgkmcnt(0)
	v_mfma_f32_16x16x32_bf16 v[120:123], v[124:127], v[36:39], v[120:123]
	ds_read_b128 v[126:129], v53 offset:26176
	s_nop 6
	v_pk_add_f32 v[108:109], v[122:123], v[108:109]
	v_pk_add_f32 v[110:111], v[120:121], v[110:111]
	v_pk_mul_f32 v[120:121], v[108:109], v[108:109]
	v_pk_mul_f32 v[114:115], v[110:111], v[110:111]
	s_nop 0
	v_pk_mov_b32 v[122:123], v[114:115], v[120:121] op_sel:[1,0]
	v_mov_b32_e32 v115, v121
	v_pk_add_f32 v[120:121], v[122:123], v[114:115]
	ds_read_b128 v[122:125], v53 offset:26112
	s_waitcnt lgkmcnt(0)
	v_mfma_f32_16x16x32_bf16 v[122:125], v[122:125], v[48:51], 0
	v_lshlrev_b32_e32 v114, 16, v112
	v_and_b32_e32 v115, 0xffff0000, v112
	v_lshlrev_b32_e32 v112, 16, v113
	v_mfma_f32_16x16x32_bf16 v[122:125], v[126:129], v[44:47], v[122:125]
	ds_read_b128 v[126:129], v53 offset:26240
	v_and_b32_e32 v113, 0xffff0000, v113
	s_waitcnt lgkmcnt(0)
	v_mfma_f32_16x16x32_bf16 v[122:125], v[126:129], v[40:43], v[122:125]
	ds_read_b128 v[126:129], v53 offset:26304
	s_waitcnt lgkmcnt(0)
	v_mfma_f32_16x16x32_bf16 v[122:125], v[126:129], v[36:39], v[122:125]
	s_nop 7
	v_pk_add_f32 v[112:113], v[124:125], v[112:113]
	v_pk_add_f32 v[114:115], v[122:123], v[114:115]
	ds_read_b128 v[122:125], v53 offset:30464
	s_waitcnt lgkmcnt(0)
	v_mfma_f32_16x16x32_bf16 v[48:51], v[122:125], v[48:51], 0
	ds_read_b128 v[122:125], v53 offset:30528
	s_waitcnt lgkmcnt(0)
	v_mfma_f32_16x16x32_bf16 v[44:47], v[122:125], v[44:47], v[48:51]
	s_nop 4
	ds_read_b128 v[48:51], v53 offset:30592
	s_waitcnt lgkmcnt(0)
	v_mfma_f32_16x16x32_bf16 v[40:43], v[48:51], v[40:43], v[44:47]
	s_nop 2
	ds_read_b128 v[44:47], v53 offset:30656
	v_lshlrev_b32_e32 v50, 16, v83
	v_and_b32_e32 v51, 0xffff0000, v83
	s_waitcnt lgkmcnt(0)
	v_mfma_f32_16x16x32_bf16 v[38:41], v[44:47], v[36:39], v[40:43]
	s_nop 2
	v_lshlrev_b32_e32 v42, 16, v116
	v_and_b32_e32 v43, 0xffff0000, v116
	v_lshlrev_b32_e32 v36, 16, v117
	v_and_b32_e32 v37, 0xffff0000, v117
	s_nop 0
	v_pk_add_f32 v[38:39], v[38:39], v[42:43]
	v_pk_add_f32 v[36:37], v[40:41], v[36:37]
	v_mul_f32_e32 v2, v38, v38
	v_mul_f32_e32 v44, v39, v39
	v_pk_add_f32 v[40:41], v[118:119], v[118:119] op_sel:[0,1] op_sel_hi:[1,0]
	v_pk_add_f32 v[42:43], v[120:121], v[120:121] op_sel:[0,1] op_sel_hi:[1,0]
	v_mov_b32_e32 v41, v2
	v_mov_b32_e32 v43, v44
	v_mul_f32_e32 v2, v115, v115
	v_mul_f32_e32 v45, v36, v36
	v_pk_add_f32 v[40:41], v[40:41], v[42:43]
	v_pk_fma_f32 v[42:43], v[114:115], v[114:115], v[2:3] op_sel_hi:[1,1,0]
	v_mul_f32_e32 v2, v113, v113
	v_mul_f32_e32 v46, v37, v37
	v_mov_b32_e32 v43, v45
	v_pk_fma_f32 v[44:45], v[112:113], v[112:113], v[2:3] op_sel_hi:[1,1,0]
	v_and_b32_e32 v47, 0xffff0000, v82
	v_mov_b32_e32 v45, v46
	v_pk_add_f32 v[42:43], v[42:43], v[44:45]
	v_lshlrev_b32_e32 v46, 16, v82
	v_pk_add_f32 v[40:41], v[40:41], v[42:43]
	v_mul_f32_e32 v48, 0xbfb8aa3b, v46
	v_add_f32_e32 v2, v40, v41
	v_and_b32_e32 v41, 64, v229
	v_xor_b32_e32 v40, 16, v229
	v_add_u32_e32 v41, 64, v41
	v_cmp_lt_i32_e32 vcc, v40, v41
	v_mul_f32_e32 v49, 0xbfb8aa3b, v47
	v_mul_f32_e32 v82, 0xbfb8aa3b, v50
	v_cndmask_b32_e32 v40, v229, v40, vcc
	v_lshlrev_b32_e32 v40, 2, v40
	ds_bpermute_b32 v40, v40, v2
	v_mul_f32_e32 v83, 0xbfb8aa3b, v51
	v_exp_f32_e32 v48, v48
	v_exp_f32_e32 v49, v49
	v_exp_f32_e32 v82, v82
	s_waitcnt lgkmcnt(0)
	v_add_f32_e32 v2, v2, v40
	v_xor_b32_e32 v40, 32, v229
	v_cmp_lt_i32_e32 vcc, v40, v41
	v_exp_f32_e32 v83, v83
	v_add_f32_e32 v48, 1.0, v48
	v_cndmask_b32_e32 v40, v229, v40, vcc
	v_lshlrev_b32_e32 v40, 2, v40
	ds_bpermute_b32 v40, v40, v2
	v_add_f32_e32 v49, 1.0, v49
	v_add_f32_e32 v82, 1.0, v82
	v_add_f32_e32 v83, 1.0, v83
	v_rcp_f32_e32 v48, v48
	s_waitcnt lgkmcnt(0)
	v_add_f32_e32 v2, v2, v40
	v_fmamk_f32 v2, v2, 0x3c000000, v230
	v_cmp_gt_f32_e32 vcc, s2, v2
	v_mul_f32_e32 v40, 0x4f800000, v2
	v_rcp_f32_e32 v49, v49
	v_cndmask_b32_e32 v2, v2, v40, vcc
	v_sqrt_f32_e32 v40, v2
	v_rcp_f32_e32 v82, v82
	v_rcp_f32_e32 v83, v83
	v_pk_mul_f32 v[46:47], v[48:49], v[46:47]
	v_add_u32_e32 v41, -1, v40
	v_fma_f32 v42, -v41, v40, v2
	v_cmp_ge_f32_e64 s[2:3], 0, v42
	v_add_u32_e32 v42, 1, v40
	v_pk_mul_f32 v[48:49], v[82:83], v[50:51]
	v_cndmask_b32_e64 v41, v40, v41, s[2:3]
	v_fma_f32 v40, -v42, v40, v2
	v_cmp_lt_f32_e64 s[2:3], 0, v40
	s_nop 1
	v_cndmask_b32_e64 v40, v41, v42, s[2:3]
	v_mul_f32_e32 v41, 0x37800000, v40
	v_cndmask_b32_e32 v40, v40, v41, vcc
	v_cmp_class_f32_e32 vcc, v2, v231
	s_nop 1
	v_cndmask_b32_e32 v2, v40, v2, vcc
	v_div_scale_f32 v40, s[2:3], v2, v2, 1.0
	v_rcp_f32_e32 v41, v40
	s_nop 0
	v_fma_f32 v42, -v40, v41, 1.0
	v_fmac_f32_e32 v41, v42, v41
	v_div_scale_f32 v42, vcc, 1.0, v2, 1.0
	v_mul_f32_e32 v43, v42, v41
	v_fma_f32 v44, -v40, v43, v42
	v_fmac_f32_e32 v43, v44, v41
	v_fma_f32 v40, -v40, v43, v42
	v_div_fmas_f32 v40, v40, v41, v43
	v_div_fixup_f32 v2, v40, v2, 1.0
	v_lshl_add_u64 v[40:41], v[62:63], 0, s[34:35]
	v_pk_mul_f32 v[50:51], v[92:93], v[2:3] op_sel_hi:[1,0]
	v_pk_mul_f32 v[82:83], v[94:95], v[2:3] op_sel_hi:[1,0]
	v_pk_mul_f32 v[36:37], v[36:37], v[2:3] op_sel_hi:[1,0]
	v_pk_mul_f32 v[38:39], v[38:39], v[2:3] op_sel_hi:[1,0]
	s_andn2_b64 vcc, exec, s[4:5]
	s_waitcnt vmcnt(0)
	v_pk_mul_f32 v[42:43], v[152:153], v[82:83]
	v_pk_mul_f32 v[44:45], v[154:155], v[50:51]
	v_pk_mul_f32 v[42:43], v[46:47], v[42:43]
	v_pk_mul_f32 v[44:45], v[48:49], v[44:45]
	v_cvt_pk_bf16_f32 v46, v42, v43
	v_cvt_pk_bf16_f32 v47, v44, v45
	v_lshl_add_u64 v[42:43], v[64:65], 0, v[80:81]
	global_store_dwordx2 v[42:43], v[46:47], off
	v_lshlrev_b32_e32 v48, 16, v78
	v_and_b32_e32 v49, 0xffff0000, v78
	v_lshlrev_b32_e32 v78, 16, v79
	v_and_b32_e32 v79, 0xffff0000, v79
	v_mul_f32_e32 v50, 0xbfb8aa3b, v48
	v_mul_f32_e32 v51, 0xbfb8aa3b, v49
	v_mul_f32_e32 v80, 0xbfb8aa3b, v78
	v_mul_f32_e32 v81, 0xbfb8aa3b, v79
	v_exp_f32_e32 v50, v50
	v_exp_f32_e32 v51, v51
	v_exp_f32_e32 v80, v80
	v_exp_f32_e32 v81, v81
	v_add_f32_e32 v50, 1.0, v50
	v_add_f32_e32 v51, 1.0, v51
	v_add_f32_e32 v80, 1.0, v80
	v_add_f32_e32 v81, 1.0, v81
	v_rcp_f32_e32 v50, v50
	v_rcp_f32_e32 v51, v51
	v_rcp_f32_e32 v80, v80
	v_rcp_f32_e32 v81, v81
	v_pk_mul_f32 v[48:49], v[50:51], v[48:49]
	v_pk_mul_f32 v[50:51], v[80:81], v[78:79]
	v_pk_mul_f32 v[78:79], v[88:89], v[2:3] op_sel_hi:[1,0]
	v_pk_mul_f32 v[80:81], v[90:91], v[2:3] op_sel_hi:[1,0]
	v_pk_mul_f32 v[46:47], v[158:159], v[78:79]
	v_pk_mul_f32 v[44:45], v[156:157], v[80:81]
	v_pk_mul_f32 v[46:47], v[50:51], v[46:47]
	v_pk_mul_f32 v[44:45], v[48:49], v[44:45]
	v_lshlrev_b32_e32 v48, 16, v76
	v_cvt_pk_bf16_f32 v44, v44, v45
	v_cvt_pk_bf16_f32 v45, v46, v47
	global_store_dwordx2 v[42:43], v[44:45], off offset:32
	v_and_b32_e32 v49, 0xffff0000, v76
	v_lshlrev_b32_e32 v76, 16, v77
	v_and_b32_e32 v77, 0xffff0000, v77
	v_mul_f32_e32 v50, 0xbfb8aa3b, v48
	v_mul_f32_e32 v51, 0xbfb8aa3b, v49
	v_mul_f32_e32 v78, 0xbfb8aa3b, v76
	v_mul_f32_e32 v79, 0xbfb8aa3b, v77
	v_exp_f32_e32 v50, v50
	v_exp_f32_e32 v51, v51
	v_exp_f32_e32 v78, v78
	v_exp_f32_e32 v79, v79
	v_add_f32_e32 v50, 1.0, v50
	v_add_f32_e32 v51, 1.0, v51
	v_add_f32_e32 v78, 1.0, v78
	v_add_f32_e32 v79, 1.0, v79
	v_rcp_f32_e32 v50, v50
	v_rcp_f32_e32 v51, v51
	v_rcp_f32_e32 v78, v78
	v_rcp_f32_e32 v79, v79
	v_pk_mul_f32 v[48:49], v[50:51], v[48:49]
	v_pk_mul_f32 v[50:51], v[78:79], v[76:77]
	v_pk_mul_f32 v[76:77], v[100:101], v[2:3] op_sel_hi:[1,0]
	v_pk_mul_f32 v[78:79], v[102:103], v[2:3] op_sel_hi:[1,0]
	v_pk_mul_f32 v[46:47], v[162:163], v[76:77]
	v_pk_mul_f32 v[44:45], v[160:161], v[78:79]
	v_pk_mul_f32 v[46:47], v[50:51], v[46:47]
	v_pk_mul_f32 v[44:45], v[48:49], v[44:45]
	v_lshlrev_b32_e32 v48, 16, v74
	v_cvt_pk_bf16_f32 v44, v44, v45
	v_cvt_pk_bf16_f32 v45, v46, v47
	global_store_dwordx2 v[42:43], v[44:45], off offset:64
	v_and_b32_e32 v49, 0xffff0000, v74
	v_lshlrev_b32_e32 v74, 16, v75
	v_and_b32_e32 v75, 0xffff0000, v75
	v_mul_f32_e32 v50, 0xbfb8aa3b, v48
	v_mul_f32_e32 v51, 0xbfb8aa3b, v49
	v_mul_f32_e32 v76, 0xbfb8aa3b, v74
	v_mul_f32_e32 v77, 0xbfb8aa3b, v75
	v_exp_f32_e32 v50, v50
	v_exp_f32_e32 v51, v51
	v_exp_f32_e32 v76, v76
	v_exp_f32_e32 v77, v77
	v_add_f32_e32 v50, 1.0, v50
	v_add_f32_e32 v51, 1.0, v51
	v_add_f32_e32 v76, 1.0, v76
	v_add_f32_e32 v77, 1.0, v77
	v_rcp_f32_e32 v50, v50
	v_rcp_f32_e32 v51, v51
	v_rcp_f32_e32 v76, v76
	v_rcp_f32_e32 v77, v77
	v_pk_mul_f32 v[48:49], v[50:51], v[48:49]
	v_pk_mul_f32 v[50:51], v[76:77], v[74:75]
	v_pk_mul_f32 v[74:75], v[96:97], v[2:3] op_sel_hi:[1,0]
	v_pk_mul_f32 v[76:77], v[98:99], v[2:3] op_sel_hi:[1,0]
	v_pk_mul_f32 v[46:47], v[166:167], v[74:75]
	v_pk_mul_f32 v[44:45], v[164:165], v[76:77]
	v_pk_mul_f32 v[46:47], v[50:51], v[46:47]
	v_pk_mul_f32 v[44:45], v[48:49], v[44:45]
	v_lshlrev_b32_e32 v48, 16, v72
	v_cvt_pk_bf16_f32 v44, v44, v45
	v_cvt_pk_bf16_f32 v45, v46, v47
	global_store_dwordx2 v[42:43], v[44:45], off offset:96
	v_and_b32_e32 v49, 0xffff0000, v72
	v_lshlrev_b32_e32 v72, 16, v73
	v_and_b32_e32 v73, 0xffff0000, v73
	v_mul_f32_e32 v50, 0xbfb8aa3b, v48
	v_mul_f32_e32 v51, 0xbfb8aa3b, v49
	v_mul_f32_e32 v74, 0xbfb8aa3b, v72
	v_mul_f32_e32 v75, 0xbfb8aa3b, v73
	v_exp_f32_e32 v50, v50
	v_exp_f32_e32 v51, v51
	v_exp_f32_e32 v74, v74
	v_exp_f32_e32 v75, v75
	v_add_f32_e32 v50, 1.0, v50
	v_add_f32_e32 v51, 1.0, v51
	v_add_f32_e32 v74, 1.0, v74
	v_add_f32_e32 v75, 1.0, v75
	v_rcp_f32_e32 v50, v50
	v_rcp_f32_e32 v51, v51
	v_rcp_f32_e32 v74, v74
	v_rcp_f32_e32 v75, v75
	v_pk_mul_f32 v[48:49], v[50:51], v[48:49]
	v_pk_mul_f32 v[50:51], v[74:75], v[72:73]
	v_pk_mul_f32 v[72:73], v[104:105], v[2:3] op_sel_hi:[1,0]
	v_pk_mul_f32 v[74:75], v[106:107], v[2:3] op_sel_hi:[1,0]
	v_pk_mul_f32 v[46:47], v[170:171], v[72:73]
	v_pk_mul_f32 v[44:45], v[168:169], v[74:75]
	v_pk_mul_f32 v[46:47], v[50:51], v[46:47]
	v_pk_mul_f32 v[44:45], v[48:49], v[44:45]
	v_lshlrev_b32_e32 v48, 16, v70
	v_cvt_pk_bf16_f32 v44, v44, v45
	v_cvt_pk_bf16_f32 v45, v46, v47
	global_store_dwordx2 v[42:43], v[44:45], off offset:128
	v_and_b32_e32 v49, 0xffff0000, v70
	v_lshlrev_b32_e32 v70, 16, v71
	v_and_b32_e32 v71, 0xffff0000, v71
	v_mul_f32_e32 v50, 0xbfb8aa3b, v48
	v_mul_f32_e32 v51, 0xbfb8aa3b, v49
	v_mul_f32_e32 v72, 0xbfb8aa3b, v70
	v_mul_f32_e32 v73, 0xbfb8aa3b, v71
	v_exp_f32_e32 v50, v50
	v_exp_f32_e32 v51, v51
	v_exp_f32_e32 v72, v72
	v_exp_f32_e32 v73, v73
	v_add_f32_e32 v50, 1.0, v50
	v_add_f32_e32 v51, 1.0, v51
	v_add_f32_e32 v72, 1.0, v72
	v_add_f32_e32 v73, 1.0, v73
	v_rcp_f32_e32 v50, v50
	v_rcp_f32_e32 v51, v51
	v_rcp_f32_e32 v72, v72
	v_rcp_f32_e32 v73, v73
	v_pk_mul_f32 v[48:49], v[50:51], v[48:49]
	v_pk_mul_f32 v[50:51], v[72:73], v[70:71]
	v_pk_mul_f32 v[70:71], v[108:109], v[2:3] op_sel_hi:[1,0]
	v_pk_mul_f32 v[72:73], v[110:111], v[2:3] op_sel_hi:[1,0]
	v_pk_mul_f32 v[46:47], v[174:175], v[70:71]
	v_pk_mul_f32 v[44:45], v[172:173], v[72:73]
	v_pk_mul_f32 v[46:47], v[50:51], v[46:47]
	v_pk_mul_f32 v[44:45], v[48:49], v[44:45]
	v_lshlrev_b32_e32 v48, 16, v68
	v_cvt_pk_bf16_f32 v44, v44, v45
	v_cvt_pk_bf16_f32 v45, v46, v47
	global_store_dwordx2 v[42:43], v[44:45], off offset:160
	v_and_b32_e32 v49, 0xffff0000, v68
	v_lshlrev_b32_e32 v68, 16, v69
	v_and_b32_e32 v69, 0xffff0000, v69
	v_mul_f32_e32 v50, 0xbfb8aa3b, v48
	v_mul_f32_e32 v51, 0xbfb8aa3b, v49
	v_mul_f32_e32 v70, 0xbfb8aa3b, v68
	v_mul_f32_e32 v71, 0xbfb8aa3b, v69
	v_exp_f32_e32 v50, v50
	v_exp_f32_e32 v51, v51
	v_exp_f32_e32 v70, v70
	v_exp_f32_e32 v71, v71
	v_add_f32_e32 v50, 1.0, v50
	v_add_f32_e32 v51, 1.0, v51
	v_add_f32_e32 v70, 1.0, v70
	v_add_f32_e32 v71, 1.0, v71
	v_rcp_f32_e32 v50, v50
	v_rcp_f32_e32 v51, v51
	v_rcp_f32_e32 v70, v70
	v_rcp_f32_e32 v71, v71
	v_pk_mul_f32 v[48:49], v[50:51], v[48:49]
	v_pk_mul_f32 v[50:51], v[70:71], v[68:69]
	v_pk_mul_f32 v[68:69], v[112:113], v[2:3] op_sel_hi:[1,0]
	v_pk_mul_f32 v[70:71], v[114:115], v[2:3] op_sel_hi:[1,0]
	v_pk_mul_f32 v[46:47], v[68:69], v[178:179]
	v_pk_mul_f32 v[44:45], v[70:71], v[176:177]
	v_pk_mul_f32 v[46:47], v[50:51], v[46:47]
	v_pk_mul_f32 v[44:45], v[48:49], v[44:45]
	v_lshlrev_b32_e32 v50, 16, v67
	v_cvt_pk_bf16_f32 v44, v44, v45
	v_cvt_pk_bf16_f32 v45, v46, v47
	global_store_dwordx2 v[42:43], v[44:45], off offset:192
	v_lshlrev_b32_e32 v40, 16, v66
	v_and_b32_e32 v41, 0xffff0000, v66
	v_and_b32_e32 v51, 0xffff0000, v67
	v_mul_f32_e32 v48, 0xbfb8aa3b, v40
	v_mul_f32_e32 v49, 0xbfb8aa3b, v41
	v_mul_f32_e32 v66, 0xbfb8aa3b, v50
	v_mul_f32_e32 v67, 0xbfb8aa3b, v51
	v_exp_f32_e32 v48, v48
	v_exp_f32_e32 v49, v49
	v_exp_f32_e32 v66, v66
	v_exp_f32_e32 v67, v67
	v_add_f32_e32 v48, 1.0, v48
	v_add_f32_e32 v49, 1.0, v49
	v_add_f32_e32 v66, 1.0, v66
	v_add_f32_e32 v67, 1.0, v67
	v_rcp_f32_e32 v48, v48
	v_rcp_f32_e32 v49, v49
	v_rcp_f32_e32 v66, v66
	v_rcp_f32_e32 v67, v67
	v_pk_mul_f32 v[40:41], v[48:49], v[40:41]
	v_pk_mul_f32 v[48:49], v[66:67], v[50:51]
	v_pk_mul_f32 v[38:39], v[38:39], v[180:181]
	v_pk_mul_f32 v[36:37], v[36:37], v[182:183]
	v_pk_mul_f32 v[38:39], v[40:41], v[38:39]
	v_pk_mul_f32 v[36:37], v[48:49], v[36:37]
	v_cvt_pk_bf16_f32 v38, v38, v39
	v_cvt_pk_bf16_f32 v39, v36, v37
	global_store_dwordx2 v[42:43], v[38:39], off offset:224
	s_waitcnt lgkmcnt(0)
	s_barrier
	s_cbranch_vccz .LBB0_768
